# sliding-window unit epilogue: sink positions requested in the prologue + next-unit ticket kept in flight, with downstream code kept at the same byte phase
# baseline (speedup 1.0000x reference)
;     ...
;     const int wq = (MODE == 3) ? (wv & 3) : (MODE == 4) ? (wv & 1) : wv, mp = (MODE == 3) ? (wv >> 2) : 0, hsel = (MODE == 4) ? (wv >> 1) : 0;
;     if (MODE == 4) { slope_l2 = slp[hsel] * LOG2E; sink_l2 = snk[hsel] * LOG2E; }
;     const int qmin = q0 + 32 * wq, qidx = qmin + r32, qmax = qmin + 31;
;     int t_lo = 0; if (SWA) { t_lo = q0 - 127; t_lo = (t_lo < 0 ? 0 : t_lo) >> 7; }
;     const int t_hi = (q0 + ((MODE == 3) ? 127 : (MODE == 4) ? 63 : 255)) >> 7;
;     if (MODE == 3 && mp) kmax = kmax1;
;     const int pos_ref = ALIBI ? pos[q0] : 0;
;     bf16x8 qf[NC];
;     { const bf16_t* qr = T.q + (size_t)qidx * T.qp + 8 * hf + (mp + hsel) * DQK;
; #pragma unroll
;       for (int c = 0; c < NC; ++c) qf[c] = *(const bf16x8*)(qr + 16 * c); }
;     f32x16 ot[2];
; #pragma unroll
;     for (int i = 0; i < 16; ++i) { ot[0][i] = 0.f; ot[1][i] = 0.f; }
;     float m = SWA ? -1e30f : 0.f, l = 0.f; bool first = true;
;     ...
;     int t = DESC ? t_hi : t_lo, b0 = 0, b1 = 1;
;     {   const bool h1 = DESC ? (t > 0) : (t < t_hi); const int t1 = DESC ? t - 1 : t + 1;
;         AT_LOAD(t); AT_STORE(0);
;         if (h1) AT_LOAD(t1);
;         __syncthreads(); }
.LBB0_1038:
	s_nop 0
	v_lshlrev_b32_e32 v165, 4, v6
	v_mul_u32_u24_e32 v163, 0x90, v5
	v_mad_u32_u24 v166, v5, s48, v165
	v_lshlrev_b32_e32 v116, 2, v6
	v_lshrrev_b32_e32 v5, 2, v4
	v_mov_b32_e32 v44, v31
	v_mov_b32_e32 v45, v31
	v_mul_f32_e32 v122, 0x3fb8aa3b, v7
	v_and_or_b32 v5, v5, 3, v116
	s_movk_i32 s44, 0xc0
	v_and_b32_e32 v6, 16, v4
	v_lshlrev_b32_e32 v7, 2, v4
	v_mov_b32_e32 v30, v31
	v_mov_b32_e32 v32, v31
	v_mov_b32_e32 v33, v31
	v_mov_b32_e32 v34, v31
	v_mov_b32_e32 v35, v31
	v_mov_b32_e32 v36, v31
	v_mov_b32_e32 v37, v31
	v_mov_b32_e32 v38, v31
	v_mov_b32_e32 v39, v31
	v_mov_b32_e32 v40, v31
	v_mov_b32_e32 v41, v31
	v_mov_b32_e32 v42, v31
	v_mov_b32_e32 v43, v31
	v_mov_b64_e32 v[62:63], v[44:45]
	v_mul_lo_u32 v5, v5, s44
	v_and_or_b32 v6, v7, 12, v6
	v_lshl_add_u64 v[124:125], v[0:1], 1, s[42:43]
	v_lshl_add_u64 v[126:127], v[2:3], 1, s[42:43]
	v_readlane_b32 s42, v254, 54
	v_mov_b64_e32 v[60:61], v[42:43]
	v_mov_b64_e32 v[58:59], v[40:41]
	v_mov_b64_e32 v[56:57], v[38:39]
	v_mov_b64_e32 v[54:55], v[36:37]
	v_mov_b64_e32 v[52:53], v[34:35]
	v_mov_b64_e32 v[50:51], v[32:33]
	v_mov_b64_e32 v[48:49], v[30:31]
	v_mov_b64_e32 v[46:47], v[44:45]
	s_lshl_b32 s21, s21, 8
	v_ashrrev_i32_e32 v113, 31, v112
	s_or_b32 s28, s63, 31
	s_add_i32 s29, s63, 0xffffff80
	s_add_i32 s92, s63, 0xffffff9f
	v_add_u32_e32 v167, 0xffffff80, v112
	s_mov_b32 s44, 1
	v_mov_b32_e32 v123, v122
	v_lshl_or_b32 v168, v6, 1, v5
	s_lshl_b32 s93, s3, 7
	v_add_u32_e32 v169, s42, v4
	v_add_u32_e32 v170, 0x100, v9
	v_add_u32_e32 v171, 0x100, v8
	s_mov_b32 s94, 0
	v_mov_b32_e32 v172, 0xf149f2ca
	v_mov_b32_e32 v119, 0
	v_mov_b64_e32 v[44:45], v[42:43]
	v_mov_b64_e32 v[42:43], v[40:41]
	v_mov_b64_e32 v[40:41], v[38:39]
	v_mov_b64_e32 v[38:39], v[36:37]
	v_mov_b64_e32 v[36:37], v[34:35]
	v_mov_b64_e32 v[34:35], v[32:33]
	v_mov_b64_e32 v[32:33], v[30:31]
	s_waitcnt lgkmcnt(0)
	s_barrier
